# router logits pass: x operand loads prefetched one 512-byte group ahead (own registers), W' LDS reads one step ahead in two quads
# baseline (speedup 1.0000x reference)
.LBB0_1420:
	s_or_b64 exec, exec, s[10:11]
	v_and_b32_e32 v15, 15, v69
	v_or_b32_e32 v2, s17, v15
	v_ashrrev_i32_e32 v3, 31, v2
	v_lshlrev_b64 v[2:3], 11, v[2:3]
	v_lshl_add_u64 v[2:3], s[14:15], 0, v[2:3]
	v_and_b32_e32 v208, 0x70, v69
	v_lshrrev_b32_e32 v14, 4, v69
	v_lshl_add_u64 v[2:3], v[2:3], 0, v[208:209]
	s_mov_b64 s[4:5], 0x26d00000
	v_lshl_add_u64 v[10:11], v[2:3], 0, s[4:5]
	v_lshlrev_b32_e32 v1, 7, v14
	v_lshlrev_b32_e32 v2, 3, v15
	v_add3_u32 v16, 0, v1, v2
	s_mov_b32 s4, 0
	v_mov_b64_e32 v[12:13], v[10:11]
	v_mov_b32_e32 v1, v0
	v_mov_b32_e32 v2, v0
	v_mov_b32_e32 v3, v0
	v_mov_b32_e32 v4, v0
	v_mov_b32_e32 v5, v0
	v_mov_b32_e32 v6, v0
	v_mov_b32_e32 v7, v0
	global_load_dwordx4 v[160:163], v[12:13], off
	global_load_dwordx4 v[164:167], v[12:13], off offset:64
	global_load_dwordx4 v[168:171], v[12:13], off offset:128
	global_load_dwordx4 v[172:175], v[12:13], off offset:192
	global_load_dwordx4 v[176:179], v[12:13], off offset:256
	global_load_dwordx4 v[180:183], v[12:13], off offset:320
	global_load_dwordx4 v[184:187], v[12:13], off offset:384
	global_load_dwordx4 v[188:191], v[12:13], off offset:448
.LBB0_1421:
	s_add_i32 s5, s4, 8
	s_cmp_lt_u32 s4, 24
	s_cselect_b64 s[10:11], -1, 0
	s_and_b64 vcc, s[10:11], exec
	s_cselect_b32 s10, s5, s4
	s_lshl_b32 s68, s10, 6
	s_mov_b32 s4, s5
	ds_read2st64_b64 v[22:25], v16 offset1:1
	s_waitcnt vmcnt(0)
	v_mov_b64_e32 v[128:129], v[160:161]
	v_mov_b64_e32 v[130:131], v[162:163]
	v_mov_b64_e32 v[132:133], v[164:165]
	v_mov_b64_e32 v[134:135], v[166:167]
	v_mov_b64_e32 v[136:137], v[168:169]
	v_mov_b64_e32 v[138:139], v[170:171]
	v_mov_b64_e32 v[140:141], v[172:173]
	v_mov_b64_e32 v[142:143], v[174:175]
	v_mov_b64_e32 v[144:145], v[176:177]
	v_mov_b64_e32 v[146:147], v[178:179]
	v_mov_b64_e32 v[148:149], v[180:181]
	v_mov_b64_e32 v[150:151], v[182:183]
	v_mov_b64_e32 v[152:153], v[184:185]
	v_mov_b64_e32 v[154:155], v[186:187]
	v_mov_b64_e32 v[156:157], v[188:189]
	v_mov_b64_e32 v[158:159], v[190:191]
	s_cbranch_vccz .Lroute_nopf
	v_lshl_add_u64 v[12:13], v[10:11], 0, s[68:69]
	global_load_dwordx4 v[160:163], v[12:13], off
	global_load_dwordx4 v[164:167], v[12:13], off offset:64
	global_load_dwordx4 v[168:171], v[12:13], off offset:128
	global_load_dwordx4 v[172:175], v[12:13], off offset:192
	global_load_dwordx4 v[176:179], v[12:13], off offset:256
	global_load_dwordx4 v[180:183], v[12:13], off offset:320
	global_load_dwordx4 v[184:187], v[12:13], off offset:384
	global_load_dwordx4 v[188:191], v[12:13], off offset:448
.Lroute_nopf:
	ds_read2st64_b64 v[192:195], v16 offset0:2 offset1:3
	v_lshlrev_b32_e32 v17, 16, v128
	s_waitcnt lgkmcnt(1)
	s_nop 0
	v_mfma_f32_16x16x4_f32 v[0:3], v17, v22, v[0:3]
	v_mfma_f32_16x16x4_f32 v[4:7], v17, v23, v[4:7]
	v_and_b32_e32 v196, 0xffff0000, v128
	s_nop 1
	v_mfma_f32_16x16x4_f32 v[0:3], v196, v24, v[0:3]
	v_mfma_f32_16x16x4_f32 v[4:7], v196, v25, v[4:7]
	ds_read2st64_b64 v[22:25], v16 offset0:4 offset1:5
	v_lshlrev_b32_e32 v17, 16, v129
	s_waitcnt lgkmcnt(1)
	s_nop 0
	v_mfma_f32_16x16x4_f32 v[0:3], v17, v192, v[0:3]
	v_mfma_f32_16x16x4_f32 v[4:7], v17, v193, v[4:7]
	v_and_b32_e32 v196, 0xffff0000, v129
	s_nop 1
	v_mfma_f32_16x16x4_f32 v[0:3], v196, v194, v[0:3]
	v_mfma_f32_16x16x4_f32 v[4:7], v196, v195, v[4:7]
	ds_read2st64_b64 v[192:195], v16 offset0:6 offset1:7
	v_lshlrev_b32_e32 v17, 16, v130
	s_waitcnt lgkmcnt(1)
	s_nop 0
	v_mfma_f32_16x16x4_f32 v[0:3], v17, v22, v[0:3]
	v_mfma_f32_16x16x4_f32 v[4:7], v17, v23, v[4:7]
	v_and_b32_e32 v196, 0xffff0000, v130
	s_nop 1
	v_mfma_f32_16x16x4_f32 v[0:3], v196, v24, v[0:3]
	v_mfma_f32_16x16x4_f32 v[4:7], v196, v25, v[4:7]
	ds_read2st64_b64 v[22:25], v16 offset0:8 offset1:9
	v_lshlrev_b32_e32 v17, 16, v131
	s_waitcnt lgkmcnt(1)
	s_nop 0
	v_mfma_f32_16x16x4_f32 v[0:3], v17, v192, v[0:3]
	v_mfma_f32_16x16x4_f32 v[4:7], v17, v193, v[4:7]
	v_and_b32_e32 v196, 0xffff0000, v131
	s_nop 1
	v_mfma_f32_16x16x4_f32 v[0:3], v196, v194, v[0:3]
	v_mfma_f32_16x16x4_f32 v[4:7], v196, v195, v[4:7]
	ds_read2st64_b64 v[192:195], v16 offset0:10 offset1:11
	v_lshlrev_b32_e32 v17, 16, v132
	s_waitcnt lgkmcnt(1)
	s_nop 0
	v_mfma_f32_16x16x4_f32 v[0:3], v17, v22, v[0:3]
	v_mfma_f32_16x16x4_f32 v[4:7], v17, v23, v[4:7]
	v_and_b32_e32 v196, 0xffff0000, v132
	s_nop 1
	v_mfma_f32_16x16x4_f32 v[0:3], v196, v24, v[0:3]
	v_mfma_f32_16x16x4_f32 v[4:7], v196, v25, v[4:7]
	ds_read2st64_b64 v[22:25], v16 offset0:12 offset1:13
	v_lshlrev_b32_e32 v17, 16, v133
	s_waitcnt lgkmcnt(1)
	s_nop 0
	v_mfma_f32_16x16x4_f32 v[0:3], v17, v192, v[0:3]
	v_mfma_f32_16x16x4_f32 v[4:7], v17, v193, v[4:7]
	v_and_b32_e32 v196, 0xffff0000, v133
	s_nop 1
	v_mfma_f32_16x16x4_f32 v[0:3], v196, v194, v[0:3]
	v_mfma_f32_16x16x4_f32 v[4:7], v196, v195, v[4:7]
	ds_read2st64_b64 v[192:195], v16 offset0:14 offset1:15
	v_lshlrev_b32_e32 v17, 16, v134
	s_waitcnt lgkmcnt(1)
	s_nop 0
	v_mfma_f32_16x16x4_f32 v[0:3], v17, v22, v[0:3]
	v_mfma_f32_16x16x4_f32 v[4:7], v17, v23, v[4:7]
	v_and_b32_e32 v196, 0xffff0000, v134
	s_nop 1
	v_mfma_f32_16x16x4_f32 v[0:3], v196, v24, v[0:3]
	v_mfma_f32_16x16x4_f32 v[4:7], v196, v25, v[4:7]
	ds_read2st64_b64 v[22:25], v16 offset0:16 offset1:17
	v_lshlrev_b32_e32 v17, 16, v135
	s_waitcnt lgkmcnt(1)
	s_nop 0
	v_mfma_f32_16x16x4_f32 v[0:3], v17, v192, v[0:3]
	v_mfma_f32_16x16x4_f32 v[4:7], v17, v193, v[4:7]
	v_and_b32_e32 v196, 0xffff0000, v135
	s_nop 1
	v_mfma_f32_16x16x4_f32 v[0:3], v196, v194, v[0:3]
	v_mfma_f32_16x16x4_f32 v[4:7], v196, v195, v[4:7]
	ds_read2st64_b64 v[192:195], v16 offset0:18 offset1:19
	v_lshlrev_b32_e32 v17, 16, v136
	s_waitcnt lgkmcnt(1)
	s_nop 0
	v_mfma_f32_16x16x4_f32 v[0:3], v17, v22, v[0:3]
	v_mfma_f32_16x16x4_f32 v[4:7], v17, v23, v[4:7]
	v_and_b32_e32 v196, 0xffff0000, v136
	s_nop 1
	v_mfma_f32_16x16x4_f32 v[0:3], v196, v24, v[0:3]
	v_mfma_f32_16x16x4_f32 v[4:7], v196, v25, v[4:7]
	ds_read2st64_b64 v[22:25], v16 offset0:20 offset1:21
	v_lshlrev_b32_e32 v17, 16, v137
	s_waitcnt lgkmcnt(1)
	s_nop 0
	v_mfma_f32_16x16x4_f32 v[0:3], v17, v192, v[0:3]
	v_mfma_f32_16x16x4_f32 v[4:7], v17, v193, v[4:7]
	v_and_b32_e32 v196, 0xffff0000, v137
	s_nop 1
	v_mfma_f32_16x16x4_f32 v[0:3], v196, v194, v[0:3]
	v_mfma_f32_16x16x4_f32 v[4:7], v196, v195, v[4:7]
	ds_read2st64_b64 v[192:195], v16 offset0:22 offset1:23
	v_lshlrev_b32_e32 v17, 16, v138
	s_waitcnt lgkmcnt(1)
	s_nop 0
	v_mfma_f32_16x16x4_f32 v[0:3], v17, v22, v[0:3]
	v_mfma_f32_16x16x4_f32 v[4:7], v17, v23, v[4:7]
	v_and_b32_e32 v196, 0xffff0000, v138
	s_nop 1
	v_mfma_f32_16x16x4_f32 v[0:3], v196, v24, v[0:3]
	v_mfma_f32_16x16x4_f32 v[4:7], v196, v25, v[4:7]
	ds_read2st64_b64 v[22:25], v16 offset0:24 offset1:25
	v_lshlrev_b32_e32 v17, 16, v139
	s_waitcnt lgkmcnt(1)
	s_nop 0
	v_mfma_f32_16x16x4_f32 v[0:3], v17, v192, v[0:3]
	v_mfma_f32_16x16x4_f32 v[4:7], v17, v193, v[4:7]
	v_and_b32_e32 v196, 0xffff0000, v139
	s_nop 1
	v_mfma_f32_16x16x4_f32 v[0:3], v196, v194, v[0:3]
	v_mfma_f32_16x16x4_f32 v[4:7], v196, v195, v[4:7]
	ds_read2st64_b64 v[192:195], v16 offset0:26 offset1:27
	v_lshlrev_b32_e32 v17, 16, v140
	s_waitcnt lgkmcnt(1)
	s_nop 0
	v_mfma_f32_16x16x4_f32 v[0:3], v17, v22, v[0:3]
	v_mfma_f32_16x16x4_f32 v[4:7], v17, v23, v[4:7]
	v_and_b32_e32 v196, 0xffff0000, v140
	s_nop 1
	v_mfma_f32_16x16x4_f32 v[0:3], v196, v24, v[0:3]
	v_mfma_f32_16x16x4_f32 v[4:7], v196, v25, v[4:7]
	ds_read2st64_b64 v[22:25], v16 offset0:28 offset1:29
	v_lshlrev_b32_e32 v17, 16, v141
	s_waitcnt lgkmcnt(1)
	s_nop 0
	v_mfma_f32_16x16x4_f32 v[0:3], v17, v192, v[0:3]
	v_mfma_f32_16x16x4_f32 v[4:7], v17, v193, v[4:7]
	v_and_b32_e32 v196, 0xffff0000, v141
	s_nop 1
	v_mfma_f32_16x16x4_f32 v[0:3], v196, v194, v[0:3]
	v_mfma_f32_16x16x4_f32 v[4:7], v196, v195, v[4:7]
	ds_read2st64_b64 v[192:195], v16 offset0:30 offset1:31
	v_lshlrev_b32_e32 v17, 16, v142
	s_waitcnt lgkmcnt(1)
	s_nop 0
	v_mfma_f32_16x16x4_f32 v[0:3], v17, v22, v[0:3]
	v_mfma_f32_16x16x4_f32 v[4:7], v17, v23, v[4:7]
	v_and_b32_e32 v196, 0xffff0000, v142
	s_nop 1
	v_mfma_f32_16x16x4_f32 v[0:3], v196, v24, v[0:3]
	v_mfma_f32_16x16x4_f32 v[4:7], v196, v25, v[4:7]
	ds_read2st64_b64 v[22:25], v16 offset0:32 offset1:33
	v_lshlrev_b32_e32 v17, 16, v143
	s_waitcnt lgkmcnt(1)
	s_nop 0
	v_mfma_f32_16x16x4_f32 v[0:3], v17, v192, v[0:3]
	v_mfma_f32_16x16x4_f32 v[4:7], v17, v193, v[4:7]
	v_and_b32_e32 v196, 0xffff0000, v143
	s_nop 1
	v_mfma_f32_16x16x4_f32 v[0:3], v196, v194, v[0:3]
	v_mfma_f32_16x16x4_f32 v[4:7], v196, v195, v[4:7]
	ds_read2st64_b64 v[192:195], v16 offset0:34 offset1:35
	v_lshlrev_b32_e32 v17, 16, v144
	s_waitcnt lgkmcnt(1)
	s_nop 0
	v_mfma_f32_16x16x4_f32 v[0:3], v17, v22, v[0:3]
	v_mfma_f32_16x16x4_f32 v[4:7], v17, v23, v[4:7]
	v_and_b32_e32 v196, 0xffff0000, v144
	s_nop 1
	v_mfma_f32_16x16x4_f32 v[0:3], v196, v24, v[0:3]
	v_mfma_f32_16x16x4_f32 v[4:7], v196, v25, v[4:7]
	ds_read2st64_b64 v[22:25], v16 offset0:36 offset1:37
	v_lshlrev_b32_e32 v17, 16, v145
	s_waitcnt lgkmcnt(1)
	s_nop 0
	v_mfma_f32_16x16x4_f32 v[0:3], v17, v192, v[0:3]
	v_mfma_f32_16x16x4_f32 v[4:7], v17, v193, v[4:7]
	v_and_b32_e32 v196, 0xffff0000, v145
	s_nop 1
	v_mfma_f32_16x16x4_f32 v[0:3], v196, v194, v[0:3]
	v_mfma_f32_16x16x4_f32 v[4:7], v196, v195, v[4:7]
	ds_read2st64_b64 v[192:195], v16 offset0:38 offset1:39
	v_lshlrev_b32_e32 v17, 16, v146
	s_waitcnt lgkmcnt(1)
	s_nop 0
	v_mfma_f32_16x16x4_f32 v[0:3], v17, v22, v[0:3]
	v_mfma_f32_16x16x4_f32 v[4:7], v17, v23, v[4:7]
	v_and_b32_e32 v196, 0xffff0000, v146
	s_nop 1
	v_mfma_f32_16x16x4_f32 v[0:3], v196, v24, v[0:3]
	v_mfma_f32_16x16x4_f32 v[4:7], v196, v25, v[4:7]
	ds_read2st64_b64 v[22:25], v16 offset0:40 offset1:41
	v_lshlrev_b32_e32 v17, 16, v147
	s_waitcnt lgkmcnt(1)
	s_nop 0
	v_mfma_f32_16x16x4_f32 v[0:3], v17, v192, v[0:3]
	v_mfma_f32_16x16x4_f32 v[4:7], v17, v193, v[4:7]
	v_and_b32_e32 v196, 0xffff0000, v147
	s_nop 1
	v_mfma_f32_16x16x4_f32 v[0:3], v196, v194, v[0:3]
	v_mfma_f32_16x16x4_f32 v[4:7], v196, v195, v[4:7]
	ds_read2st64_b64 v[192:195], v16 offset0:42 offset1:43
	v_lshlrev_b32_e32 v17, 16, v148
	s_waitcnt lgkmcnt(1)
	s_nop 0
	v_mfma_f32_16x16x4_f32 v[0:3], v17, v22, v[0:3]
	v_mfma_f32_16x16x4_f32 v[4:7], v17, v23, v[4:7]
	v_and_b32_e32 v196, 0xffff0000, v148
	s_nop 1
	v_mfma_f32_16x16x4_f32 v[0:3], v196, v24, v[0:3]
	v_mfma_f32_16x16x4_f32 v[4:7], v196, v25, v[4:7]
	ds_read2st64_b64 v[22:25], v16 offset0:44 offset1:45
	v_lshlrev_b32_e32 v17, 16, v149
	s_waitcnt lgkmcnt(1)
	s_nop 0
	v_mfma_f32_16x16x4_f32 v[0:3], v17, v192, v[0:3]
	v_mfma_f32_16x16x4_f32 v[4:7], v17, v193, v[4:7]
	v_and_b32_e32 v196, 0xffff0000, v149
	s_nop 1
	v_mfma_f32_16x16x4_f32 v[0:3], v196, v194, v[0:3]
	v_mfma_f32_16x16x4_f32 v[4:7], v196, v195, v[4:7]
	ds_read2st64_b64 v[192:195], v16 offset0:46 offset1:47
	v_lshlrev_b32_e32 v17, 16, v150
	s_waitcnt lgkmcnt(1)
	s_nop 0
	v_mfma_f32_16x16x4_f32 v[0:3], v17, v22, v[0:3]
	v_mfma_f32_16x16x4_f32 v[4:7], v17, v23, v[4:7]
	v_and_b32_e32 v196, 0xffff0000, v150
	s_nop 1
	v_mfma_f32_16x16x4_f32 v[0:3], v196, v24, v[0:3]
	v_mfma_f32_16x16x4_f32 v[4:7], v196, v25, v[4:7]
	ds_read2st64_b64 v[22:25], v16 offset0:48 offset1:49
	v_lshlrev_b32_e32 v17, 16, v151
	s_waitcnt lgkmcnt(1)
	s_nop 0
	v_mfma_f32_16x16x4_f32 v[0:3], v17, v192, v[0:3]
	v_mfma_f32_16x16x4_f32 v[4:7], v17, v193, v[4:7]
	v_and_b32_e32 v196, 0xffff0000, v151
	s_nop 1
	v_mfma_f32_16x16x4_f32 v[0:3], v196, v194, v[0:3]
	v_mfma_f32_16x16x4_f32 v[4:7], v196, v195, v[4:7]
	ds_read2st64_b64 v[192:195], v16 offset0:50 offset1:51
	v_lshlrev_b32_e32 v17, 16, v152
	s_waitcnt lgkmcnt(1)
	s_nop 0
	v_mfma_f32_16x16x4_f32 v[0:3], v17, v22, v[0:3]
	v_mfma_f32_16x16x4_f32 v[4:7], v17, v23, v[4:7]
	v_and_b32_e32 v196, 0xffff0000, v152
	s_nop 1
	v_mfma_f32_16x16x4_f32 v[0:3], v196, v24, v[0:3]
	v_mfma_f32_16x16x4_f32 v[4:7], v196, v25, v[4:7]
	ds_read2st64_b64 v[22:25], v16 offset0:52 offset1:53
	v_lshlrev_b32_e32 v17, 16, v153
	s_waitcnt lgkmcnt(1)
	s_nop 0
	v_mfma_f32_16x16x4_f32 v[0:3], v17, v192, v[0:3]
	v_mfma_f32_16x16x4_f32 v[4:7], v17, v193, v[4:7]
	v_and_b32_e32 v196, 0xffff0000, v153
	s_nop 1
	v_mfma_f32_16x16x4_f32 v[0:3], v196, v194, v[0:3]
	v_mfma_f32_16x16x4_f32 v[4:7], v196, v195, v[4:7]
	ds_read2st64_b64 v[192:195], v16 offset0:54 offset1:55
	v_lshlrev_b32_e32 v17, 16, v154
	s_waitcnt lgkmcnt(1)
	s_nop 0
	v_mfma_f32_16x16x4_f32 v[0:3], v17, v22, v[0:3]
	v_mfma_f32_16x16x4_f32 v[4:7], v17, v23, v[4:7]
	v_and_b32_e32 v196, 0xffff0000, v154
	s_nop 1
	v_mfma_f32_16x16x4_f32 v[0:3], v196, v24, v[0:3]
	v_mfma_f32_16x16x4_f32 v[4:7], v196, v25, v[4:7]
	ds_read2st64_b64 v[22:25], v16 offset0:56 offset1:57
	v_lshlrev_b32_e32 v17, 16, v155
	s_waitcnt lgkmcnt(1)
	s_nop 0
	v_mfma_f32_16x16x4_f32 v[0:3], v17, v192, v[0:3]
	v_mfma_f32_16x16x4_f32 v[4:7], v17, v193, v[4:7]
	v_and_b32_e32 v196, 0xffff0000, v155
	s_nop 1
	v_mfma_f32_16x16x4_f32 v[0:3], v196, v194, v[0:3]
	v_mfma_f32_16x16x4_f32 v[4:7], v196, v195, v[4:7]
	ds_read2st64_b64 v[192:195], v16 offset0:58 offset1:59
	v_lshlrev_b32_e32 v17, 16, v156
	s_waitcnt lgkmcnt(1)
	s_nop 0
	v_mfma_f32_16x16x4_f32 v[0:3], v17, v22, v[0:3]
	v_mfma_f32_16x16x4_f32 v[4:7], v17, v23, v[4:7]
	v_and_b32_e32 v196, 0xffff0000, v156
	s_nop 1
	v_mfma_f32_16x16x4_f32 v[0:3], v196, v24, v[0:3]
	v_mfma_f32_16x16x4_f32 v[4:7], v196, v25, v[4:7]
	ds_read2st64_b64 v[22:25], v16 offset0:60 offset1:61
	v_lshlrev_b32_e32 v17, 16, v157
	s_waitcnt lgkmcnt(1)
	s_nop 0
	v_mfma_f32_16x16x4_f32 v[0:3], v17, v192, v[0:3]
	v_mfma_f32_16x16x4_f32 v[4:7], v17, v193, v[4:7]
	v_and_b32_e32 v196, 0xffff0000, v157
	s_nop 1
	v_mfma_f32_16x16x4_f32 v[0:3], v196, v194, v[0:3]
	v_mfma_f32_16x16x4_f32 v[4:7], v196, v195, v[4:7]
	ds_read2st64_b64 v[192:195], v16 offset0:62 offset1:63
	v_lshlrev_b32_e32 v17, 16, v158
	s_waitcnt lgkmcnt(1)
	s_nop 0
	v_mfma_f32_16x16x4_f32 v[0:3], v17, v22, v[0:3]
	v_mfma_f32_16x16x4_f32 v[4:7], v17, v23, v[4:7]
	v_and_b32_e32 v196, 0xffff0000, v158
	s_nop 1
	v_mfma_f32_16x16x4_f32 v[0:3], v196, v24, v[0:3]
	v_mfma_f32_16x16x4_f32 v[4:7], v196, v25, v[4:7]
	v_lshlrev_b32_e32 v17, 16, v159
	s_waitcnt lgkmcnt(0)
	s_nop 0
	v_mfma_f32_16x16x4_f32 v[0:3], v17, v192, v[0:3]
	v_mfma_f32_16x16x4_f32 v[4:7], v17, v193, v[4:7]
	v_and_b32_e32 v196, 0xffff0000, v159
	s_nop 1
	v_mfma_f32_16x16x4_f32 v[0:3], v196, v194, v[0:3]
	v_mfma_f32_16x16x4_f32 v[4:7], v196, v195, v[4:7]
	v_add_u32_e32 v16, 0x8000, v16
	s_cbranch_vccnz .LBB0_1421
	s_mulk_i32 s16, 0x840
	s_add_i32 s4, s16, 0
	s_add_i32 s4, s4, 0x20000
	v_mul_u32_u24_e32 v10, 0x210, v14
	v_lshlrev_b32_e32 v11, 2, v15
	v_add3_u32 v10, s4, v10, v11
	s_nop 1
	ds_write2_b32 v10, v0, v4 offset1:16
	ds_write2_b32 v10, v1, v5 offset0:33 offset1:49
	ds_write2_b32 v10, v2, v6 offset0:66 offset1:82
	ds_write2_b32 v10, v3, v7 offset0:99 offset1:115
	s_waitcnt lgkmcnt(0)
	s_and_saveexec_b64 s[16:17], s[2:3]
	s_cbranch_execz .LBB0_1428
	s_lshl_b32 s2, s12, 2
	s_ashr_i32 s3, s2, 31
	s_lshl_b64 s[2:3], s[2:3], 2
	s_add_u32 s2, s8, s2
	s_addc_u32 s3, s9, s3
	v_mov_b32_e32 v0, s4
	s_movk_i32 s4, 0x84
	v_mad_u32_u24 v6, v69, s4, v0
	global_load_dwordx4 v[0:3], v209, s[2:3]
	ds_read2_b32 v[4:5], v6 offset0:16 offset1:17
	s_lshl_b32 s8, s12, 4
	s_ashr_i32 s9, s8, 31
	s_lshl_b64 s[8:9], s[8:9], 2
	s_add_u32 s6, s6, s8
	s_addc_u32 s7, s7, s9
	s_mov_b32 s10, 0xff800000
	s_waitcnt vmcnt(0) lgkmcnt(0)
	v_fma_f32 v10, v8, v4, v0
	v_max_f32_e32 v4, 0xff800000, v10
	v_fma_f32 v0, v8, v5, v1
	v_cmp_gt_f32_e64 s[2:3], v0, v4
	s_nop 1
	v_cndmask_b32_e64 v1, v4, v0, s[2:3]
	ds_read2_b32 v[4:5], v6 offset0:18 offset1:19
	s_waitcnt lgkmcnt(0)
	v_fma_f32 v2, v8, v4, v2
	v_cmp_gt_f32_e64 s[4:5], v2, v1
	v_fmac_f32_e32 v3, v8, v5
	s_nop 0
	v_cndmask_b32_e64 v11, v1, v2, s[4:5]
	v_cndmask_b32_e64 v1, 0, 1, s[2:3]
	v_cmp_gt_f32_e32 vcc, v3, v11
	v_cndmask_b32_e64 v1, v1, 2, s[4:5]
	s_nop 0
	v_cndmask_b32_e64 v1, v1, 3, vcc
	v_lshlrev_b32_e32 v4, 4, v1
	v_add_u32_e32 v14, v6, v4
	global_load_dwordx4 v[4:7], v4, s[6:7]
	ds_read2_b32 v[12:13], v14 offset1:1
	s_waitcnt vmcnt(0) lgkmcnt(0)
	v_pk_fma_f32 v[12:13], v[8:9], v[12:13], v[4:5] op_sel_hi:[0,1,1]
	ds_read2_b32 v[4:5], v14 offset0:2 offset1:3
	v_cmp_gt_f32_e64 s[2:3], v13, v12
	v_cmp_nlg_f32_e64 s[10:11], s10, v12
	s_waitcnt lgkmcnt(0)
	v_fma_f32 v6, v8, v4, v6
	v_cndmask_b32_e64 v4, v12, v13, s[2:3]
	v_cmp_ngt_f32_e64 s[4:5], v6, v4
	v_fmac_f32_e32 v7, v8, v5
	v_cndmask_b32_e64 v14, 0, 1, s[2:3]
	v_cndmask_b32_e64 v5, v6, v4, s[4:5]
	v_cndmask_b32_e64 v4, 2, v14, s[4:5]
	v_cmp_gt_f32_e64 s[6:7], v7, v5
	v_cmp_ngt_f32_e64 s[2:3], v7, v5
	s_nop 0
	v_cndmask_b32_e64 v4, v4, 3, s[6:7]
	v_cmp_eq_u32_e64 s[8:9], 0, v4
	s_or_b64 s[8:9], s[8:9], s[10:11]
	s_or_b64 s[6:7], s[4:5], s[6:7]
	v_cndmask_b32_e64 v12, v12, v230, s[8:9]
	v_cndmask_b32_e64 v14, 0, -1, s[8:9]
	v_cmp_ne_u32_e64 s[8:9], 1, v4
	v_cmp_gt_f32_e64 s[10:11], v13, v12
	s_and_b64 s[8:9], s[8:9], s[10:11]
	v_cndmask_b32_e64 v12, v12, v13, s[8:9]
	v_cmp_gt_f32_e64 s[4:5], v6, v12
	v_cndmask_b32_e64 v13, v14, 1, s[8:9]
	s_and_b64 s[4:5], s[6:7], s[4:5]
	v_cndmask_b32_e64 v12, v12, v6, s[4:5]
	v_cndmask_b32_e64 v6, v13, 2, s[4:5]
	s_and_saveexec_b64 s[4:5], s[2:3]
	s_cbranch_execz .LBB0_1427
	v_cmp_gt_f32_e64 s[2:3], v7, v12
	s_and_saveexec_b64 s[6:7], s[2:3]
	v_mov_b32_e32 v6, 3
	v_mov_b32_e32 v12, v7
	s_or_b64 exec, exec, s[6:7]
	v_mov_b32_e32 v7, v5
